# v36 + the ten GEMM K-loop heads (back-edge targets) aligned to 64 bytes with s_nop padding
# baseline (speedup 1.0000x reference)
.LBB0_430:
	s_add_i32 s9, s6, 0xffff8000
	s_and_b32 s9, s9, 0x8000
	s_add_i32 s9, s9, 0
	s_add_i32 s8, s5, 0
	s_add_i32 s9, s9, 0x18000
	v_add_u32_e32 v204, s9, v153
	v_add_u32_e32 v206, s8, v169
	v_add_u32_e32 v212, s9, v151
	v_add_u32_e32 v208, s9, v152
	.p2alignl 6, 3212836864

.LBB0_877:
	s_lshl_b32 s6, s38, 10
	s_and_b32 s6, s6, 0x40000
	s_lshl_b64 s[24:25], s[2:3], 18
	s_add_u32 s52, s36, s24
	v_readfirstlane_b32 s24, v0
	s_addc_u32 s53, s37, s25
	s_lshr_b32 s25, s24, 6
	v_or_b32_e32 v176, s6, v168
	s_lshl_b32 s6, s25, 1
	v_or_b32_e32 v2, s6, v1
	s_and_b32 s26, s25, 4
	s_bfe_u32 s3, s24, 0x20006
	v_and_or_b32 v3, v2, 3, s26
	s_lshr_b32 s26, s24, 1
	s_and_b32 s50, s26, 0x7fffff80
	s_lshl_b32 s26, s3, 7
	s_lshl_b32 s51, s25, 10
	s_waitcnt vmcnt(0)
	s_barrier
	s_or_b32 s27, s26, 32
	s_add_i32 s51, s51, 0
	s_mov_b32 s25, m0
	s_mov_b32 m0, s51
	s_nop 0
	global_load_lds_dwordx4 v21, s[22:23]
	s_mov_b32 m0, s25
	v_bitop3_b32 v173, s26, v167, v161 bitop3:0xde
	v_bitop3_b32 v172, s27, v167, v161 bitop3:0xde
	s_or_b32 s27, s26, 64
	s_or_b32 s26, s26, 0x60
	s_add_i32 s25, s51, 0x2000
	v_bitop3_b32 v169, s26, v167, v161 bitop3:0xde
	s_mov_b32 s26, m0
	s_mov_b32 m0, s25
	s_nop 0
	global_load_lds_dwordx4 v20, s[22:23]
	s_mov_b32 m0, s26
	s_add_i32 s25, s51, 0x4000
	s_mov_b32 s26, m0
	s_mov_b32 m0, s25
	s_nop 0
	global_load_lds_dwordx4 v19, s[22:23]
	s_mov_b32 m0, s26
	s_add_i32 s25, s51, 0x6000
	s_mov_b32 s26, m0
	s_mov_b32 m0, s25
	s_nop 0
	global_load_lds_dwordx4 v18, s[22:23]
	s_mov_b32 m0, s26
	v_bitop3_b32 v171, s27, v167, v161 bitop3:0xde
	s_lshl_b64 s[26:27], s[6:7], 9
	s_add_u32 s26, s52, s26
	v_lshlrev_b32_e32 v3, 5, v3
	v_or_b32_e32 v4, s50, v154
	v_lshlrev_b32_e32 v2, 9, v2
	s_addc_u32 s27, s53, s27
	v_lshlrev_b32_e32 v34, 7, v4
	v_bitop3_b32 v174, v3, v2, v157 bitop3:0xde
	global_load_dwordx4 v[2:5], v151, s[26:27]
	s_add_i32 s26, s6, 16
	s_mov_b32 s27, s7
	s_lshl_b64 s[26:27], s[26:27], 9
	s_add_u32 s26, s52, s26
	s_addc_u32 s27, s53, s27
	global_load_dwordx4 v[6:9], v151, s[26:27]
	s_add_i32 s26, s6, 32
	s_mov_b32 s27, s7
	s_lshl_b64 s[26:27], s[26:27], 9
	s_add_u32 s26, s52, s26
	s_addc_u32 s27, s53, s27
	global_load_dwordx4 v[10:13], v151, s[26:27]
	s_add_i32 s26, s6, 48
	s_mov_b32 s27, s7
	s_lshl_b64 s[26:27], s[26:27], 9
	s_add_u32 s26, s52, s26
	s_addc_u32 s27, s53, s27
	s_add_i32 s25, s51, 0x8000
	global_load_dwordx4 v[14:17], v151, s[26:27]
	s_mov_b32 s26, m0
	s_mov_b32 m0, s25
	s_nop 0
	global_load_lds_dwordx4 v25, s[22:23]
	s_mov_b32 m0, s26
	s_add_i32 s25, s51, 0xa000
	s_mov_b32 s26, m0
	s_mov_b32 m0, s25
	s_nop 0
	global_load_lds_dwordx4 v22, s[22:23]
	s_mov_b32 m0, s26
	s_add_i32 s25, s51, 0xc000
	s_mov_b32 s26, m0
	s_mov_b32 m0, s25
	s_nop 0
	global_load_lds_dwordx4 v23, s[22:23]
	s_mov_b32 m0, s26
	s_add_i32 s25, s51, 0xe000
	s_mov_b32 s26, m0
	s_mov_b32 m0, s25
	s_nop 0
	global_load_lds_dwordx4 v24, s[22:23]
	s_mov_b32 m0, s26
	s_add_i32 s26, s6, 64
	s_mov_b32 s27, s7
	s_waitcnt vmcnt(4)
	s_lshl_b64 s[26:27], s[26:27], 9
	v_add_u32_e32 v18, 0, v174
	s_add_u32 s26, s52, s26
	v_add_u32_e32 v178, 0x18000, v18
	s_addc_u32 s27, s53, s27
	ds_write_b128 v178, v[2:5]
	ds_write_b128 v178, v[6:9] offset:8192
	ds_write_b128 v178, v[10:13] offset:16384
	ds_write_b128 v178, v[14:17] offset:24576
	global_load_dwordx4 v[14:17], v151, s[26:27]
	s_add_i32 s26, s6, 0x50
	s_mov_b32 s27, s7
	s_lshl_b64 s[26:27], s[26:27], 9
	s_add_u32 s26, s52, s26
	s_addc_u32 s27, s53, s27
	global_load_dwordx4 v[10:13], v151, s[26:27]
	s_add_i32 s26, s6, 0x60
	s_mov_b32 s27, s7
	s_lshl_b64 s[26:27], s[26:27], 9
	s_add_u32 s26, s52, s26
	s_addc_u32 s27, s53, s27
	s_addk_i32 s6, 0x70
	global_load_dwordx4 v[6:9], v151, s[26:27]
	s_lshl_b64 s[26:27], s[6:7], 9
	s_add_u32 s26, s52, s26
	s_addc_u32 s27, s53, s27
	s_lshl_b64 s[24:25], s[24:25], 4
	global_load_dwordx4 v[2:5], v151, s[26:27]
	s_waitcnt lgkmcnt(0)
	s_barrier
	s_and_b32 s25, s25, 15
	s_and_b32 s6, s24, 0xfffffc00
	s_add_u32 s6, s52, s6
	v_mov_b32_e32 v18, 0
	v_or_b32_e32 v175, v34, v159
	v_or_b32_e32 v177, v34, v156
	s_addc_u32 s52, s53, s25
	s_mov_b32 s53, 0x10000
	s_mov_b32 s73, 0
	s_mov_b64 s[24:25], 0
	v_mov_b32_e32 v19, v18
	v_mov_b32_e32 v20, v18
	v_mov_b32_e32 v21, v18
	v_mov_b32_e32 v22, v18
	v_mov_b32_e32 v23, v18
	v_mov_b32_e32 v24, v18
	v_mov_b32_e32 v25, v18
	v_mov_b32_e32 v26, v18
	v_mov_b32_e32 v27, v18
	v_mov_b32_e32 v28, v18
	v_mov_b32_e32 v29, v18
	v_mov_b32_e32 v30, v18
	v_mov_b32_e32 v31, v18
	v_mov_b32_e32 v32, v18
	v_mov_b32_e32 v33, v18
	v_mov_b32_e32 v34, v18
	v_mov_b32_e32 v35, v18
	v_mov_b32_e32 v36, v18
	v_mov_b32_e32 v37, v18
	v_mov_b32_e32 v38, v18
	v_mov_b32_e32 v39, v18
	v_mov_b32_e32 v40, v18
	v_mov_b32_e32 v41, v18
	v_mov_b32_e32 v46, v18
	v_mov_b32_e32 v47, v18
	v_mov_b32_e32 v48, v18
	v_mov_b32_e32 v49, v18
	v_mov_b32_e32 v62, v18
	v_mov_b32_e32 v63, v18
	v_mov_b32_e32 v64, v18
	v_mov_b32_e32 v65, v18
	v_mov_b32_e32 v66, v18
	v_mov_b32_e32 v67, v18
	v_mov_b32_e32 v68, v18
	v_mov_b32_e32 v69, v18
	v_mov_b32_e32 v78, v18
	v_mov_b32_e32 v79, v18
	v_mov_b32_e32 v80, v18
	v_mov_b32_e32 v81, v18
	v_mov_b32_e32 v90, v18
	v_mov_b32_e32 v91, v18
	v_mov_b32_e32 v92, v18
	v_mov_b32_e32 v93, v18
	v_mov_b32_e32 v94, v18
	v_mov_b32_e32 v95, v18
	v_mov_b32_e32 v96, v18
	v_mov_b32_e32 v97, v18
	v_mov_b32_e32 v114, v18
	v_mov_b32_e32 v115, v18
	v_mov_b32_e32 v116, v18
	v_mov_b32_e32 v117, v18
	v_mov_b32_e32 v122, v18
	v_mov_b32_e32 v123, v18
	v_mov_b32_e32 v124, v18
	v_mov_b32_e32 v125, v18
	v_mov_b32_e32 v138, v18
	v_mov_b32_e32 v139, v18
	v_mov_b32_e32 v140, v18
	v_mov_b32_e32 v141, v18
	v_mov_b32_e32 v142, v18
	v_mov_b32_e32 v143, v18
	v_mov_b32_e32 v144, v18
	v_mov_b32_e32 v145, v18
	v_mov_b32_e32 v118, v18
	v_mov_b32_e32 v119, v18
	v_mov_b32_e32 v120, v18
	v_mov_b32_e32 v121, v18
	v_mov_b32_e32 v126, v18
	v_mov_b32_e32 v127, v18
	v_mov_b32_e32 v128, v18
	v_mov_b32_e32 v129, v18
	v_mov_b32_e32 v134, v18
	v_mov_b32_e32 v135, v18
	v_mov_b32_e32 v136, v18
	v_mov_b32_e32 v137, v18
	v_mov_b32_e32 v130, v18
	v_mov_b32_e32 v131, v18
	v_mov_b32_e32 v132, v18
	v_mov_b32_e32 v133, v18
	v_mov_b32_e32 v98, v18
	v_mov_b32_e32 v99, v18
	v_mov_b32_e32 v100, v18
	v_mov_b32_e32 v101, v18
	v_mov_b32_e32 v102, v18
	v_mov_b32_e32 v103, v18
	v_mov_b32_e32 v104, v18
	v_mov_b32_e32 v105, v18
	v_mov_b32_e32 v110, v18
	v_mov_b32_e32 v111, v18
	v_mov_b32_e32 v112, v18
	v_mov_b32_e32 v113, v18
	v_mov_b32_e32 v106, v18
	v_mov_b32_e32 v107, v18
	v_mov_b32_e32 v108, v18
	v_mov_b32_e32 v109, v18
	v_mov_b32_e32 v70, v18
	v_mov_b32_e32 v71, v18
	v_mov_b32_e32 v72, v18
	v_mov_b32_e32 v73, v18
	v_mov_b32_e32 v82, v18
	v_mov_b32_e32 v83, v18
	v_mov_b32_e32 v84, v18
	v_mov_b32_e32 v85, v18
	v_mov_b32_e32 v86, v18
	v_mov_b32_e32 v87, v18
	v_mov_b32_e32 v88, v18
	v_mov_b32_e32 v89, v18
	v_mov_b32_e32 v74, v18
	v_mov_b32_e32 v75, v18
	v_mov_b32_e32 v76, v18
	v_mov_b32_e32 v77, v18
	v_mov_b32_e32 v42, v18
	v_mov_b32_e32 v43, v18
	v_mov_b32_e32 v44, v18
	v_mov_b32_e32 v45, v18
	v_mov_b32_e32 v54, v18
	v_mov_b32_e32 v55, v18
	v_mov_b32_e32 v56, v18
	v_mov_b32_e32 v57, v18
	v_mov_b32_e32 v58, v18
	v_mov_b32_e32 v59, v18
	v_mov_b32_e32 v60, v18
	v_mov_b32_e32 v61, v18
	v_mov_b32_e32 v50, v18
	v_mov_b32_e32 v51, v18
	v_mov_b32_e32 v52, v18
	v_mov_b32_e32 v53, v18
	.p2alignl 6, 3212836864

.LBB0_947:
	s_or_b64 exec, exec, s[0:1]
	s_add_u32 s0, s70, 0x9038000
	s_addc_u32 s1, s71, 0
	s_ashr_i32 s22, s96, 2
	s_and_b32 s2, s22, 0xfffff8
	s_and_b32 s23, s96, 7
	s_bfe_u32 s8, s96, 0x20003
	s_or_b32 s2, s2, s23
	s_lshl_b32 s6, s8, 8
	s_lshl_b32 s4, s8, 9
	s_add_u32 s4, s70, s4
	s_addc_u32 s5, s71, 0
	s_add_u32 s24, s4, 0x20168000
	v_readfirstlane_b32 s4, v0
	s_addc_u32 s25, s5, 0
	s_lshr_b32 s10, s4, 6
	s_lshl_b32 s9, s2, 8
	s_lshl_b32 s2, s10, 1
	s_waitcnt vmcnt(23)
	v_lshlrev_b32_e32 v2, 4, v164
	v_or_b32_e32 v5, s2, v1
	s_and_b32 s5, s10, 4
	v_and_b32_e32 v146, 0x70, v2
	v_or_b32_e32 v2, s9, v147
	s_waitcnt vmcnt(7)
	v_and_or_b32 v6, v5, 3, s5
	s_lshr_b32 s5, s4, 1
	s_lshl_b32 s7, s10, 10
	s_barrier
	s_waitcnt vmcnt(4)
	v_lshl_or_b32 v18, v2, 11, v146
	s_and_b32 s16, s5, 0x7fffff80
	s_add_i32 s7, s7, 0
	s_mov_b32 s5, m0
	s_mov_b32 m0, s7
	s_nop 0
	global_load_lds_dwordx4 v18, s[0:1]
	s_mov_b32 m0, s5
	s_add_i32 s5, s7, 0x2000
	v_or_b32_e32 v2, 0x20000, v18
	s_mov_b32 s18, m0
	s_mov_b32 m0, s5
	s_nop 0
	global_load_lds_dwordx4 v2, s[0:1]
	s_mov_b32 m0, s18
	s_add_i32 s5, s7, 0x4000
	s_mov_b32 s3, 0
	v_or_b32_e32 v3, 0x40000, v18
	v_or_b32_e32 v4, 0x60000, v18
	s_bfe_u32 s17, s4, 0x20006
	s_mov_b32 s18, m0
	s_mov_b32 m0, s5
	s_nop 0
	global_load_lds_dwordx4 v3, s[0:1]
	s_mov_b32 m0, s18
	s_add_i32 s5, s7, 0x6000
	s_mov_b32 s18, m0
	s_mov_b32 m0, s5
	s_nop 0
	global_load_lds_dwordx4 v4, s[0:1]
	s_mov_b32 m0, s18
	s_lshl_b32 s11, s17, 7
	s_lshl_b64 s[18:19], s[2:3], 11
	s_add_u32 s18, s24, s18
	v_lshlrev_b32_e32 v6, 5, v6
	v_xor_b32_e32 v8, s11, v161
	v_lshlrev_b32_e32 v5, 9, v5
	s_addc_u32 s19, s25, s19
	v_lshl_or_b32 v163, v1, 11, v157
	v_or3_b32 v152, v162, v8, v160
	v_bitop3_b32 v8, s11, v161, 32 bitop3:0x36
	v_bitop3_b32 v157, v6, v5, v157 bitop3:0xde
	global_load_dwordx4 v[2:5], v163, s[18:19]
	s_add_i32 s18, s2, 16
	s_mov_b32 s19, s3
	v_or3_b32 v151, v162, v8, v160
	v_bitop3_b32 v8, s11, v161, 64 bitop3:0x36
	s_lshl_b64 s[18:19], s[18:19], 11
	v_or3_b32 v149, v162, v8, v160
	v_mov_b32_e32 v8, 0x60
	s_add_u32 s18, s24, s18
	v_or_b32_e32 v7, s16, v154
	v_bitop3_b32 v8, s11, v161, v8 bitop3:0x36
	s_addc_u32 s19, s25, s19
	v_or3_b32 v148, v162, v8, v160
	v_lshlrev_b32_e32 v34, 7, v7
	global_load_dwordx4 v[6:9], v163, s[18:19]
	s_add_i32 s18, s2, 32
	s_mov_b32 s19, s3
	s_lshl_b64 s[18:19], s[18:19], 11
	s_add_u32 s18, s24, s18
	s_addc_u32 s19, s25, s19
	global_load_dwordx4 v[10:13], v163, s[18:19]
	s_add_i32 s18, s2, 48
	s_mov_b32 s19, s3
	s_lshl_b64 s[18:19], s[18:19], 11
	s_add_u32 s18, s24, s18
	s_addc_u32 s19, s25, s19
	s_add_i32 s5, s7, 0x8000
	v_or_b32_e32 v19, 0x80, v18
	global_load_dwordx4 v[14:17], v163, s[18:19]
	s_mov_b32 s19, m0
	s_mov_b32 m0, s5
	s_nop 0
	global_load_lds_dwordx4 v19, s[0:1]
	s_mov_b32 m0, s19
	v_or_b32_e32 v19, 0x20080, v18
	s_add_i32 s5, s7, 0xa000
	s_mov_b32 s19, m0
	s_mov_b32 m0, s5
	s_nop 0
	global_load_lds_dwordx4 v19, s[0:1]
	s_mov_b32 m0, s19
	v_or_b32_e32 v19, 0x40080, v18
	s_add_i32 s5, s7, 0xc000
	v_or_b32_e32 v18, 0x60080, v18
	s_add_i32 s20, s2, 64
	s_mov_b32 s21, s3
	s_mov_b32 s19, m0
	s_mov_b32 m0, s5
	s_nop 0
	global_load_lds_dwordx4 v19, s[0:1]
	s_mov_b32 m0, s19
	s_add_i32 s5, s7, 0xe000
	s_mov_b32 s19, m0
	s_mov_b32 m0, s5
	s_nop 0
	global_load_lds_dwordx4 v18, s[0:1]
	s_mov_b32 m0, s19
	s_waitcnt vmcnt(2)
	s_waitcnt vmcnt(4)
	s_lshl_b64 s[20:21], s[20:21], 11
	v_add_u32_e32 v18, 0, v157
	s_add_u32 s20, s24, s20
	v_or_b32_e32 v150, v34, v159
	v_add_u32_e32 v159, 0x18000, v18
	s_addc_u32 s21, s25, s21
	ds_write_b128 v159, v[2:5]
	ds_write_b128 v159, v[6:9] offset:8192
	ds_write_b128 v159, v[10:13] offset:16384
	ds_write_b128 v159, v[14:17] offset:24576
	global_load_dwordx4 v[14:17], v163, s[20:21]
	s_add_i32 s20, s2, 0x50
	s_mov_b32 s21, s3
	s_lshl_b64 s[20:21], s[20:21], 11
	s_add_u32 s20, s24, s20
	s_addc_u32 s21, s25, s21
	global_load_dwordx4 v[10:13], v163, s[20:21]
	s_add_i32 s20, s2, 0x60
	s_mov_b32 s21, s3
	s_lshl_b64 s[20:21], s[20:21], 11
	s_add_u32 s20, s24, s20
	s_addc_u32 s21, s25, s21
	s_addk_i32 s2, 0x70
	global_load_dwordx4 v[6:9], v163, s[20:21]
	s_lshl_b64 s[20:21], s[2:3], 11
	s_add_u32 s20, s24, s20
	s_addc_u32 s21, s25, s21
	s_lshl_b64 s[4:5], s[4:5], 6
	s_and_b32 s5, s5, 63
	s_and_b32 s2, s4, 0xfffff000
	s_add_u32 s2, s24, s2
	s_addc_u32 s19, s25, s5
	s_lshl_b32 s4, s22, 19
	s_and_b32 s4, s4, 0xffc00000
	s_lshl_b32 s5, s23, 19
	global_load_dwordx4 v[2:5], v163, s[20:21]
	s_or_b32 s20, s4, s5
	v_lshlrev_b32_e32 v18, 11, v147
	s_waitcnt lgkmcnt(0)
	s_barrier
	v_or_b32_e32 v147, s20, v18
	v_or_b32_e32 v18, s4, v18
	v_or_b32_e32 v153, v34, v156
	v_or_b32_e32 v156, s5, v18
	v_mov_b32_e32 v18, 0
	s_mov_b32 s18, 0x8000
	s_mov_b32 s20, 0x10000
	s_mov_b64 s[4:5], 0
	v_mov_b32_e32 v19, v18
	v_mov_b32_e32 v20, v18
	v_mov_b32_e32 v21, v18
	v_mov_b32_e32 v30, v18
	v_mov_b32_e32 v31, v18
	v_mov_b32_e32 v32, v18
	v_mov_b32_e32 v33, v18
	v_mov_b32_e32 v22, v18
	v_mov_b32_e32 v23, v18
	v_mov_b32_e32 v24, v18
	v_mov_b32_e32 v25, v18
	v_mov_b32_e32 v26, v18
	v_mov_b32_e32 v27, v18
	v_mov_b32_e32 v28, v18
	v_mov_b32_e32 v29, v18
	v_mov_b32_e32 v34, v18
	v_mov_b32_e32 v35, v18
	v_mov_b32_e32 v36, v18
	v_mov_b32_e32 v37, v18
	s_waitcnt vmcnt(1)
	v_mov_b32_e32 v38, v18
	v_mov_b32_e32 v39, v18
	v_mov_b32_e32 v40, v18
	v_mov_b32_e32 v41, v18
	s_waitcnt vmcnt(0)
	v_mov_b32_e32 v42, v18
	v_mov_b32_e32 v43, v18
	v_mov_b32_e32 v44, v18
	v_mov_b32_e32 v45, v18
	v_mov_b32_e32 v50, v18
	v_mov_b32_e32 v51, v18
	v_mov_b32_e32 v52, v18
	v_mov_b32_e32 v53, v18
	v_mov_b32_e32 v66, v18
	v_mov_b32_e32 v67, v18
	v_mov_b32_e32 v68, v18
	v_mov_b32_e32 v69, v18
	v_mov_b32_e32 v78, v18
	v_mov_b32_e32 v79, v18
	v_mov_b32_e32 v80, v18
	v_mov_b32_e32 v81, v18
	v_mov_b32_e32 v90, v18
	v_mov_b32_e32 v91, v18
	v_mov_b32_e32 v92, v18
	v_mov_b32_e32 v93, v18
	v_mov_b32_e32 v94, v18
	v_mov_b32_e32 v95, v18
	v_mov_b32_e32 v96, v18
	v_mov_b32_e32 v97, v18
	v_mov_b32_e32 v118, v18
	v_mov_b32_e32 v119, v18
	v_mov_b32_e32 v120, v18
	v_mov_b32_e32 v121, v18
	v_mov_b32_e32 v126, v18
	v_mov_b32_e32 v127, v18
	v_mov_b32_e32 v128, v18
	v_mov_b32_e32 v129, v18
	v_mov_b32_e32 v138, v18
	v_mov_b32_e32 v139, v18
	v_mov_b32_e32 v140, v18
	v_mov_b32_e32 v141, v18
	v_mov_b32_e32 v142, v18
	v_mov_b32_e32 v143, v18
	v_mov_b32_e32 v144, v18
	v_mov_b32_e32 v145, v18
	v_mov_b32_e32 v114, v18
	v_mov_b32_e32 v115, v18
	v_mov_b32_e32 v116, v18
	v_mov_b32_e32 v117, v18
	v_mov_b32_e32 v122, v18
	v_mov_b32_e32 v123, v18
	v_mov_b32_e32 v124, v18
	v_mov_b32_e32 v125, v18
	v_mov_b32_e32 v134, v18
	v_mov_b32_e32 v135, v18
	v_mov_b32_e32 v136, v18
	v_mov_b32_e32 v137, v18
	v_mov_b32_e32 v130, v18
	v_mov_b32_e32 v131, v18
	v_mov_b32_e32 v132, v18
	v_mov_b32_e32 v133, v18
	v_mov_b32_e32 v98, v18
	v_mov_b32_e32 v99, v18
	v_mov_b32_e32 v100, v18
	v_mov_b32_e32 v101, v18
	v_mov_b32_e32 v102, v18
	v_mov_b32_e32 v103, v18
	v_mov_b32_e32 v104, v18
	v_mov_b32_e32 v105, v18
	v_mov_b32_e32 v110, v18
	v_mov_b32_e32 v111, v18
	v_mov_b32_e32 v112, v18
	v_mov_b32_e32 v113, v18
	v_mov_b32_e32 v106, v18
	v_mov_b32_e32 v107, v18
	v_mov_b32_e32 v108, v18
	v_mov_b32_e32 v109, v18
	v_mov_b32_e32 v70, v18
	v_mov_b32_e32 v71, v18
	v_mov_b32_e32 v72, v18
	v_mov_b32_e32 v73, v18
	v_mov_b32_e32 v82, v18
	v_mov_b32_e32 v83, v18
	v_mov_b32_e32 v84, v18
	v_mov_b32_e32 v85, v18
	v_mov_b32_e32 v86, v18
	v_mov_b32_e32 v87, v18
	v_mov_b32_e32 v88, v18
	v_mov_b32_e32 v89, v18
	v_mov_b32_e32 v74, v18
	v_mov_b32_e32 v75, v18
	v_mov_b32_e32 v76, v18
	v_mov_b32_e32 v77, v18
	v_mov_b32_e32 v46, v18
	v_mov_b32_e32 v47, v18
	v_mov_b32_e32 v48, v18
	v_mov_b32_e32 v49, v18
	v_mov_b32_e32 v58, v18
	v_mov_b32_e32 v59, v18
	v_mov_b32_e32 v60, v18
	v_mov_b32_e32 v61, v18
	v_mov_b32_e32 v62, v18
	v_mov_b32_e32 v63, v18
	v_mov_b32_e32 v64, v18
	v_mov_b32_e32 v65, v18
	v_mov_b32_e32 v54, v18
	v_mov_b32_e32 v55, v18
	v_mov_b32_e32 v56, v18
	v_mov_b32_e32 v57, v18
	.p2alignl 6, 3212836864

.LBB0_1039:
	s_add_i32 s34, s29, 0xffff8000
	s_and_b32 s34, s34, 0x8000
	s_add_i32 s34, s34, 0
	s_add_i32 s33, s30, 0
	s_add_i32 s34, s34, 0x18000
	v_add_u32_e32 v157, s34, v152
	v_add_u32_e32 v169, s33, v150
	v_add_u32_e32 v200, s34, v149
	v_add_u32_e32 v168, s34, v151
	.p2alignl 6, 3212836864

.LBB0_1129:
	s_add_i32 s50, s26, 0xffff8000
	s_and_b32 s50, s50, 0x8000
	s_add_i32 s50, s50, 0
	s_add_i32 s49, s8, 0
	s_add_i32 s50, s50, 0x18000
	v_add_u32_e32 v154, s50, v157
	v_add_u32_e32 v218, s49, v161
	v_add_u32_e32 v224, s50, v155
	v_add_u32_e32 v185, s50, v156
	.p2alignl 6, 3212836864

.LBB0_1131:
	s_add_i32 s50, s48, 0xffff8000
	s_and_b32 s50, s50, 0x8000
	s_add_i32 s50, s50, 0
	s_add_i32 s49, s26, 0
	s_add_i32 s50, s50, 0x18000
	v_add_u32_e32 v154, s50, v157
	v_add_u32_e32 v165, s49, v161
	v_add_u32_e32 v222, s50, v155
	v_add_u32_e32 v164, s50, v156
	.p2alignl 6, 3212836864

.LBB0_1433:
	s_add_i32 s88, s39, 0xffff8000
	s_and_b32 s88, s88, 0x8000
	s_add_i32 s88, s88, 0
	s_add_i32 s87, s86, 0
	s_add_i32 s88, s88, 0x18000
	v_add_u32_e32 v246, s88, v212
	v_add_u32_e32 v247, s87, v215
	v_add_u32_e32 v252, s88, v181
	v_add_u32_e32 v254, s88, v172
	v_add_u32_e32 v250, s88, v183
	.p2alignl 6, 3212836864

.LBB0_1446:
	s_add_i32 s87, s37, 0xffff8000
	s_and_b32 s87, s87, 0x8000
	s_add_i32 s87, s87, 0
	s_add_i32 s86, s85, 0
	s_add_i32 s87, s87, 0x18000
	v_add_u32_e32 v240, s87, v185
	v_add_u32_e32 v241, s86, v183
	v_add_u32_e32 v246, s87, v181
	v_add_u32_e32 v248, s87, v172
	v_add_u32_e32 v244, s87, v184
	.p2alignl 6, 3212836864

.LBB0_1478:
	s_add_i32 s59, s34, 0xffff8000
	s_and_b32 s59, s59, 0x8000
	s_add_i32 s59, s59, 0
	s_add_i32 s41, s40, 0
	s_add_i32 s59, s59, 0x18000
	v_add_u32_e32 v236, s59, v184
	v_add_u32_e32 v237, s41, v187
	v_add_u32_e32 v242, s59, v181
	v_add_u32_e32 v244, s59, v172
	v_add_u32_e32 v240, s59, v183
	.p2alignl 6, 3212836864

.LBB0_1540:
	s_add_i32 s42, s37, 0xffff8000
	s_and_b32 s42, s42, 0x8000
	s_add_i32 s41, s40, 0
	s_add_i32 s42, s24, s42
	v_add_u32_e32 v234, s42, v183
	v_add_u32_e32 v235, s41, v207
	v_add_u32_e32 v240, s42, v179
	v_add_u32_e32 v242, s42, v172
	v_add_u32_e32 v238, s42, v181
	.p2alignl 6, 3212836864
